# baseline (speedup 1.0000x reference)
_ZN12_GLOBAL__N_113search_kernelEPKfS1_PhPf:
	s_load_dwordx2 s[8:9], s[0:1], 0x0
	s_load_dwordx2 s[4:5], s[0:1], 0x10
	s_movk_i32 s3, 0x90
	v_readfirstlane_b32 s10, v0
	v_cmp_gt_u32_e32 vcc, s3, v0
	s_and_saveexec_b64 s[6:7], vcc
	v_mov_b32_e32 v2, -1
	v_lshlrev_b32_e32 v1, 3, v0
	v_mov_b32_e32 v3, v2
	ds_write_b64 v1, v[2:3] offset:16384
	s_or_b64 exec, exec, s[6:7]
	s_waitcnt lgkmcnt(0)
	s_add_u32 s6, s4, 0x240000
	s_addc_u32 s7, s5, 0
	s_lshl_b32 s11, s2, 1
	s_and_b32 s14, s11, 14
	s_ashr_i32 s11, s2, 7
	s_lshr_b32 s15, s10, 6
	s_add_i32 s14, s14, s11
	s_bfe_u32 s2, s2, 0x40003
	s_mul_i32 s11, s15, 24
	v_mul_u32_u24_e32 v2, 0x71d, v0
	v_mul_u32_u24_e32 v4, 0x195, v0
	s_min_u32 s18, s11, 0xa5
	s_mul_i32 s11, s14, 3
	s_mul_i32 s12, s2, 9
	s_mov_b32 s13, 0
	v_lshrrev_b32_e32 v3, 16, v2
	s_movk_i32 s19, 0xffdc
	v_lshrrev_b32_e32 v5, 17, v4
	v_mad_i32_i24 v2, v3, s19, v0
	v_mad_i32_i24 v4, v5, -9, v3
	v_add_u32_e32 v3, s11, v5
	v_mov_b64_e32 v[6:7], s[12:13]
	v_mad_i64_i32 v[8:9], s[16:17], v3, s3, v[6:7]
	v_ashrrev_i32_e32 v5, 31, v4
	v_lshl_add_u64 v[4:5], v[8:9], 0, v[4:5]
	s_movk_i32 s13, 0x240
	v_mov_b64_e32 v[8:9], s[8:9]
	v_mad_u64_u32 v[10:11], s[8:9], v4, s13, v[8:9]
	v_min_u32_e32 v4, 0x1cb, v0
	v_or_b32_e32 v4, 0x200, v4
	v_mad_i32_i24 v11, v5, s13, v11
	v_mul_u32_u24_e32 v5, 0x71d, v4
	v_ashrrev_i32_e32 v3, 31, v2
	v_lshrrev_b32_e32 v5, 16, v5
	v_lshl_add_u64 v[2:3], v[2:3], 4, v[10:11]
	v_mad_i32_i24 v10, v5, s19, v4
	v_mul_u32_u24_e32 v4, 0x653, v4
	v_lshrrev_b32_e32 v11, 19, v4
	v_mad_i32_i24 v4, v11, -9, v5
	v_add_u32_e32 v5, s11, v11
	v_mad_i64_i32 v[6:7], s[8:9], v5, s3, v[6:7]
	v_ashrrev_i32_e32 v5, 31, v4
	v_lshl_add_u64 v[4:5], v[6:7], 0, v[4:5]
	v_mad_u64_u32 v[12:13], s[8:9], v4, s13, v[8:9]
	s_mul_i32 s8, s14, 0x90
	global_load_dwordx4 v[6:9], v[2:3], off
	s_add_i32 s3, s8, s12
	v_and_b32_e32 v210, 15, v0
	v_lshlrev_b32_e32 v252, 3, v210
	v_bfe_u32 v253, v0, 4, 2
	s_lshl_b32 s11, s3, 6
	v_and_b32_e32 v2, 48, v0
	s_mul_i32 s9, s14, 0xbd
	v_or3_b32 v2, s11, v2, v210
	s_add_i32 s18, s18, s9
	v_and_b32_e32 v1, 63, v0
	v_ashrrev_i32_e32 v3, 31, v2
	s_lshl_b32 s3, s18, 6
	v_mad_i32_i24 v13, v5, s13, v13
	v_lshl_add_u64 v[14:15], v[2:3], 4, s[4:5]
	v_or_b32_e32 v2, s3, v1
	v_ashrrev_i32_e32 v11, 31, v10
	v_ashrrev_i32_e32 v3, 31, v2
	v_lshl_add_u64 v[10:11], v[10:11], 4, v[12:13]
	v_lshl_add_u64 v[16:17], v[2:3], 4, s[6:7]
	global_load_dwordx4 v[2:5], v[14:15], off
	global_load_dwordx4 v[58:61], v[16:17], off nt
	s_add_i32 s12, s3, 64
	global_load_dwordx4 v[10:13], v[10:11], off
	v_or_b32_e32 v14, s12, v1
	v_ashrrev_i32_e32 v15, 31, v14
	v_lshl_add_u64 v[14:15], v[14:15], 4, s[6:7]
	s_add_i32 s12, s3, 0x80
	global_load_dwordx4 v[54:57], v[14:15], off nt
	v_or_b32_e32 v14, s12, v1
	v_ashrrev_i32_e32 v15, 31, v14
	v_lshl_add_u64 v[14:15], v[14:15], 4, s[6:7]
	s_add_i32 s12, s3, 0xc0
	global_load_dwordx4 v[98:101], v[14:15], off nt
	v_or_b32_e32 v14, s12, v1
	v_ashrrev_i32_e32 v15, 31, v14
	v_lshl_add_u64 v[14:15], v[14:15], 4, s[6:7]
	s_add_i32 s12, s11, 64
	global_load_dwordx4 v[82:85], v[14:15], off nt
	v_or_b32_e32 v14, s12, v1
	v_ashrrev_i32_e32 v15, 31, v14
	v_lshl_add_u64 v[14:15], v[14:15], 4, s[4:5]
	s_add_i32 s12, s11, 0x80
	global_load_dwordx4 v[34:37], v[14:15], off
	v_or_b32_e32 v14, s12, v1
	s_add_i32 s12, s11, 0xc0
	v_or_b32_e32 v16, s12, v1
	s_add_i32 s12, s11, 0x100
	v_or_b32_e32 v18, s12, v1
	s_add_i32 s12, s11, 0x140
	v_ashrrev_i32_e32 v15, 31, v14
	v_ashrrev_i32_e32 v17, 31, v16
	v_or_b32_e32 v20, s12, v1
	v_lshl_add_u64 v[14:15], v[14:15], 4, s[4:5]
	v_lshl_add_u64 v[16:17], v[16:17], 4, s[4:5]
	v_ashrrev_i32_e32 v21, 31, v20
	s_add_i32 s12, s11, 0x180
	global_load_dwordx4 v[30:33], v[14:15], off
	global_load_dwordx4 v[26:29], v[16:17], off
	v_lshl_add_u64 v[14:15], v[20:21], 4, s[4:5]
	v_or_b32_e32 v20, s12, v1
	v_ashrrev_i32_e32 v21, 31, v20
	s_add_i32 s12, s11, 0x1c0
	v_lshl_add_u64 v[38:39], v[20:21], 4, s[4:5]
	v_or_b32_e32 v20, s12, v1
	v_ashrrev_i32_e32 v21, 31, v20
	s_addk_i32 s11, 0x200
	v_lshl_add_u64 v[40:41], v[20:21], 4, s[4:5]
	v_or_b32_e32 v20, s11, v1
	v_ashrrev_i32_e32 v21, 31, v20
	s_add_i32 s11, s3, 0x100
	v_lshl_add_u64 v[42:43], v[20:21], 4, s[4:5]
	v_or_b32_e32 v20, s11, v1
	s_add_i32 s11, s3, 0x140
	v_or_b32_e32 v16, s11, v1
	v_ashrrev_i32_e32 v17, 31, v16
	s_add_i32 s11, s3, 0x180
	v_lshl_add_u64 v[46:47], v[16:17], 4, s[6:7]
	v_or_b32_e32 v16, s11, v1
	v_ashrrev_i32_e32 v17, 31, v16
	s_add_i32 s11, s3, 0x1c0
	v_lshl_add_u64 v[48:49], v[16:17], 4, s[6:7]
	v_or_b32_e32 v16, s11, v1
	v_ashrrev_i32_e32 v17, 31, v16
	s_add_i32 s11, s3, 0x200
	v_lshl_add_u64 v[50:51], v[16:17], 4, s[6:7]
	v_or_b32_e32 v16, s11, v1
	v_ashrrev_i32_e32 v17, 31, v16
	s_add_i32 s11, s3, 0x240
	v_lshl_add_u64 v[52:53], v[16:17], 4, s[6:7]
	v_or_b32_e32 v16, s11, v1
	v_ashrrev_i32_e32 v17, 31, v16
	s_add_i32 s11, s3, 0x280
	v_ashrrev_i32_e32 v19, 31, v18
	v_ashrrev_i32_e32 v21, 31, v20
	v_lshl_add_u64 v[66:67], v[16:17], 4, s[6:7]
	v_or_b32_e32 v16, s11, v1
	v_lshl_add_u64 v[18:19], v[18:19], 4, s[4:5]
	v_lshl_add_u64 v[44:45], v[20:21], 4, s[6:7]
	v_ashrrev_i32_e32 v17, 31, v16
	s_add_i32 s11, s3, 0x2c0
	global_load_dwordx4 v[22:25], v[18:19], off
	v_lshl_add_u64 v[86:87], v[16:17], 4, s[6:7]
	v_or_b32_e32 v16, s11, v1
	s_add_i32 s11, s3, 0x300
	global_load_dwordx4 v[18:21], v[14:15], off
	global_load_dwordx4 v[62:65], v[44:45], off nt
	v_lshlrev_b32_e32 v14, 4, v0
	s_waitcnt vmcnt(12)
	ds_write_b128 v14, v[6:9]
	v_or_b32_e32 v6, s11, v1
	v_ashrrev_i32_e32 v7, 31, v6
	s_add_i32 s11, s3, 0x340
	v_lshl_add_u64 v[142:143], v[6:7], 4, s[6:7]
	v_or_b32_e32 v6, s11, v1
	v_ashrrev_i32_e32 v7, 31, v6
	s_add_i32 s11, s3, 0x380
	v_lshl_add_u64 v[146:147], v[6:7], 4, s[6:7]
	v_or_b32_e32 v6, s11, v1
	v_ashrrev_i32_e32 v17, 31, v16
	v_ashrrev_i32_e32 v7, 31, v6
	v_lshl_add_u64 v[88:89], v[16:17], 4, s[6:7]
	s_waitcnt vmcnt(9)
	ds_write_b128 v14, v[10:13] offset:8192
	global_load_dwordx4 v[14:17], v[38:39], off
	global_load_dwordx4 v[10:13], v[40:41], off
	v_lshl_add_u64 v[38:39], v[6:7], 4, s[6:7]
	global_load_dwordx4 v[6:9], v[42:43], off
	global_load_dwordx4 v[94:97], v[46:47], off nt
	global_load_dwordx4 v[78:81], v[48:49], off nt
	global_load_dwordx4 v[74:77], v[50:51], off nt
	global_load_dwordx4 v[70:73], v[52:53], off nt
	s_add_i32 s11, s3, 0x3c0
	v_or_b32_e32 v40, s11, v1
	v_ashrrev_i32_e32 v41, 31, v40
	s_barrier
	v_mfma_f32_16x16x32_f16 v[102:105], v[58:61], v[2:5], 0
	v_lshl_add_u64 v[40:41], v[40:41], 4, s[6:7]
	global_load_dwordx4 v[66:69], v[66:67], off nt
	s_nop 0
	global_load_dwordx4 v[90:93], v[86:87], off nt
	s_nop 0
	global_load_dwordx4 v[86:89], v[88:89], off nt
	s_nop 0
	global_load_dwordx4 v[50:53], v[142:143], off nt
	global_load_dwordx4 v[46:49], v[146:147], off nt
	global_load_dwordx4 v[42:45], v[38:39], off nt
	s_nop 0
	global_load_dwordx4 v[38:41], v[40:41], off nt
	s_waitcnt vmcnt(22)
	v_mfma_f32_16x16x32_f16 v[106:109], v[54:57], v[2:5], 0
	s_mov_b32 s11, 0x7f000000
	v_mov_b32_e32 v159, 0
	v_mov_b32_e32 v171, 0
	s_waitcnt vmcnt(21)
	v_mfma_f32_16x16x32_f16 v[110:113], v[98:101], v[2:5], 0
	v_mov_b32_e32 v173, 0
	v_mov_b32_e32 v197, 0
	v_mov_b32_e32 v195, 0
	s_waitcnt vmcnt(20)
	v_mfma_f32_16x16x32_f16 v[114:117], v[82:85], v[2:5], 0
	v_mov_b32_e32 v199, 0
	v_min_i32_e32 v102, v102, v103
	v_min_i32_e32 v103, v104, v105
	v_min_i32_e32 v104, v106, v107
	v_min_i32_e32 v105, v108, v109
	v_min_i32_e32 v154, v110, v111
	v_min3_i32 v102, v102, v103, v104
	v_min_i32_e32 v155, v112, v113
	v_min_i32_e32 v114, v114, v115
	v_min3_i32 v102, v102, v105, v154
	s_waitcnt vmcnt(19)
	v_mfma_f32_16x16x32_f16 v[118:121], v[58:61], v[34:37], 0
	v_min_i32_e32 v115, v116, v117
	v_min3_i32 v102, v102, v155, v114
	v_min3_i32 v158, v102, v115, s11
	v_mfma_f32_16x16x32_f16 v[122:125], v[54:57], v[34:37], 0
	v_mov_b32_e32 v204, 0
	s_add_i32 s12, s3, 0x400
	v_mov_b32_e32 v205, 0
	v_mfma_f32_16x16x32_f16 v[126:129], v[98:101], v[34:37], 0
	v_mov_b32_e32 v220, 0
	v_mfma_f32_16x16x32_f16 v[130:133], v[82:85], v[34:37], 0
	s_waitcnt vmcnt(18)
	v_mfma_f32_16x16x32_f16 v[134:137], v[58:61], v[30:33], 0
	v_mfma_f32_16x16x32_f16 v[138:141], v[54:57], v[30:33], 0
	v_mfma_f32_16x16x32_f16 v[142:145], v[98:101], v[30:33], 0
	v_mfma_f32_16x16x32_f16 v[146:149], v[82:85], v[30:33], 0
	s_nop 0
	v_min_i32_e32 v102, v118, v119
	v_min_i32_e32 v103, v120, v121
	v_min_i32_e32 v104, v122, v123
	v_min_i32_e32 v105, v124, v125
	v_min_i32_e32 v114, v126, v127
	v_min3_i32 v102, v102, v103, v104
	v_min_i32_e32 v115, v128, v129
	v_min_i32_e32 v116, v130, v131
	v_min3_i32 v102, v102, v105, v114
	v_min_i32_e32 v117, v132, v133
	v_min3_i32 v102, v102, v115, v116
	s_waitcnt vmcnt(17)
	v_mfma_f32_16x16x32_f16 v[150:153], v[58:61], v[26:29], 0
	v_min3_i32 v170, v102, v117, s11
	v_mfma_f32_16x16x32_f16 v[106:109], v[54:57], v[26:29], 0
	v_mfma_f32_16x16x32_f16 v[110:113], v[98:101], v[26:29], 0
	v_mfma_f32_16x16x32_f16 v[154:157], v[82:85], v[26:29], 0
	s_nop 0
	v_min_i32_e32 v114, v134, v135
	v_min_i32_e32 v115, v136, v137
	v_min_i32_e32 v116, v138, v139
	v_min_i32_e32 v117, v140, v141
	v_min_i32_e32 v122, v142, v143
	v_min3_i32 v114, v114, v115, v116
	v_min_i32_e32 v123, v144, v145
	v_min_i32_e32 v124, v146, v147
	v_min3_i32 v114, v114, v117, v122
	v_min_i32_e32 v125, v148, v149
	v_min3_i32 v114, v114, v123, v124
	s_waitcnt vmcnt(16)
	v_mfma_f32_16x16x32_f16 v[160:163], v[58:61], v[22:25], 0
	v_min3_i32 v172, v114, v125, s11
	v_mfma_f32_16x16x32_f16 v[164:167], v[54:57], v[22:25], 0
	v_mfma_f32_16x16x32_f16 v[118:121], v[98:101], v[22:25], 0
	v_mfma_f32_16x16x32_f16 v[128:131], v[82:85], v[22:25], 0
	s_nop 0
	v_min_i32_e32 v110, v110, v111
	s_waitcnt vmcnt(15)
	v_mfma_f32_16x16x32_f16 v[174:177], v[58:61], v[18:21], 0
	v_min_i32_e32 v111, v112, v113
	v_min_i32_e32 v112, v154, v155
	v_min_i32_e32 v113, v156, v157
	s_waitcnt vmcnt(13)
	v_mfma_f32_16x16x32_f16 v[102:105], v[58:61], v[14:17], 0
	s_waitcnt vmcnt(12)
	v_mfma_f32_16x16x32_f16 v[134:137], v[58:61], v[10:13], 0
	s_waitcnt vmcnt(11)
	v_mfma_f32_16x16x32_f16 v[114:117], v[58:61], v[6:9], 0
	v_min_i32_e32 v58, v150, v151
	v_min_i32_e32 v59, v152, v153
	v_min_i32_e32 v60, v106, v107
	v_min_i32_e32 v61, v108, v109
	v_min3_i32 v58, v58, v59, v60
	v_min3_i32 v58, v58, v61, v110
	v_min3_i32 v58, v58, v111, v112
	v_mfma_f32_16x16x32_f16 v[178:181], v[54:57], v[18:21], 0
	v_min3_i32 v196, v58, v113, s11
	v_mfma_f32_16x16x32_f16 v[182:185], v[98:101], v[18:21], 0
	v_mfma_f32_16x16x32_f16 v[186:189], v[82:85], v[18:21], 0
	s_nop 0
	v_min_i32_e32 v110, v160, v161
	v_min_i32_e32 v111, v162, v163
	v_min_i32_e32 v112, v164, v165
	v_mfma_f32_16x16x32_f16 v[142:145], v[54:57], v[14:17], 0
	v_min_i32_e32 v113, v166, v167
	v_min_i32_e32 v118, v118, v119
	v_min_i32_e32 v119, v120, v121
	v_mfma_f32_16x16x32_f16 v[146:149], v[98:101], v[14:17], 0
	v_min_i32_e32 v120, v128, v129
	v_mfma_f32_16x16x32_f16 v[58:61], v[54:57], v[10:13], 0
	v_mfma_f32_16x16x32_f16 v[122:125], v[54:57], v[6:9], 0
	v_mfma_f32_16x16x32_f16 v[54:57], v[98:101], v[10:13], 0
	v_mfma_f32_16x16x32_f16 v[126:129], v[98:101], v[6:9], 0
	v_min3_i32 v99, v110, v111, v112
	v_min3_i32 v99, v99, v113, v118
	v_min_i32_e32 v98, v130, v131
	v_min3_i32 v99, v99, v119, v120
	v_mfma_f32_16x16x32_f16 v[106:109], v[82:85], v[14:17], 0
	v_min3_i32 v194, v99, v98, s11
	v_mfma_f32_16x16x32_f16 v[138:141], v[82:85], v[10:13], 0
	v_min_i32_e32 v98, v182, v183
	v_min_i32_e32 v99, v184, v185
	v_min_i32_e32 v100, v186, v187
	v_mfma_f32_16x16x32_f16 v[130:133], v[82:85], v[6:9], 0
	v_min_i32_e32 v82, v174, v175
	v_min_i32_e32 v83, v176, v177
	v_min_i32_e32 v84, v178, v179
	v_min_i32_e32 v85, v180, v181
	v_min3_i32 v82, v82, v83, v84
	v_min3_i32 v82, v82, v85, v98
	v_min_i32_e32 v101, v188, v189
	v_min3_i32 v82, v82, v99, v100
	v_min3_i32 v198, v82, v101, s11
	v_mfma_f32_16x16x32_f16 v[150:153], v[62:65], v[2:5], 0
	v_min_i32_e32 v82, v102, v103
	v_min_i32_e32 v83, v104, v105
	v_min_i32_e32 v84, v142, v143
	v_min_i32_e32 v85, v144, v145
	v_min_i32_e32 v98, v146, v147
	v_min3_i32 v82, v82, v83, v84
	v_min_i32_e32 v99, v148, v149
	v_min_i32_e32 v100, v106, v107
	v_min3_i32 v82, v82, v85, v98
	v_min_i32_e32 v101, v108, v109
	v_min3_i32 v82, v82, v99, v100
	v_min3_i32 v203, v82, v101, s11
	v_mfma_f32_16x16x32_f16 v[162:165], v[62:65], v[34:37], 0
	v_min_i32_e32 v58, v58, v59
	v_min_i32_e32 v59, v60, v61
	v_min_i32_e32 v54, v54, v55
	v_mfma_f32_16x16x32_f16 v[166:169], v[62:65], v[30:33], 0
	v_min_i32_e32 v55, v56, v57
	v_min_i32_e32 v56, v138, v139
	v_min_i32_e32 v57, v140, v141
	v_mfma_f32_16x16x32_f16 v[154:157], v[62:65], v[26:29], 0
	v_mfma_f32_16x16x32_f16 v[110:113], v[62:65], v[22:25], 0
	v_mfma_f32_16x16x32_f16 v[118:121], v[62:65], v[18:21], 0
	v_mfma_f32_16x16x32_f16 v[102:105], v[62:65], v[14:17], 0
	v_mfma_f32_16x16x32_f16 v[106:109], v[62:65], v[10:13], 0
	v_mfma_f32_16x16x32_f16 v[98:101], v[62:65], v[6:9], 0
	v_min_i32_e32 v62, v134, v135
	v_min_i32_e32 v63, v136, v137
	v_min3_i32 v58, v62, v63, v58
	v_min3_i32 v54, v58, v59, v54
	v_min3_i32 v54, v54, v55, v56
	v_min3_i32 v202, v54, v57, s11
	v_mov_b32_e32 v54, 0
	s_waitcnt vmcnt(10)
	v_mfma_f32_16x16x32_f16 v[174:177], v[94:97], v[2:5], 0
	v_add_u32_e32 v60, v1, v54
	v_add_u32_e32 v54, s12, v60
	s_add_i32 s12, s3, 0x440
	v_add_u32_e32 v56, s12, v60
	s_add_i32 s12, s3, 0x480
	v_add_u32_e32 v58, s12, v60
	s_add_i32 s12, s3, 0x4c0
	v_ashrrev_i32_e32 v55, 31, v54
	v_ashrrev_i32_e32 v57, 31, v56
	v_ashrrev_i32_e32 v59, 31, v58
	v_add_u32_e32 v60, s12, v60
	s_waitcnt vmcnt(9)
	v_mfma_f32_16x16x32_f16 v[134:137], v[78:81], v[2:5], 0
	v_lshl_add_u64 v[54:55], v[54:55], 4, s[6:7]
	v_lshl_add_u64 v[56:57], v[56:57], 4, s[6:7]
	v_lshl_add_u64 v[58:59], v[58:59], 4, s[6:7]
	s_waitcnt vmcnt(8)
	v_mfma_f32_16x16x32_f16 v[178:181], v[74:77], v[2:5], 0
	v_ashrrev_i32_e32 v61, 31, v60
	v_lshl_add_u64 v[138:139], v[60:61], 4, s[6:7]
	global_load_dwordx4 v[82:85], v[54:55], off nt
	global_load_dwordx4 v[62:65], v[56:57], off nt
	s_nop 0
	global_load_dwordx4 v[58:61], v[58:59], off nt
	s_nop 0
	global_load_dwordx4 v[54:57], v[138:139], off nt
	v_mfma_f32_16x16x32_f16 v[182:185], v[94:97], v[34:37], 0
	v_min_i32_e32 v114, v114, v115
	v_min_i32_e32 v115, v116, v117
	v_min_i32_e32 v116, v122, v123
	v_min_i32_e32 v117, v124, v125
	v_min_i32_e32 v122, v126, v127
	v_min3_i32 v114, v114, v115, v116
	v_min_i32_e32 v123, v128, v129
	v_min_i32_e32 v124, v130, v131
	v_min3_i32 v114, v114, v117, v122
	v_min_i32_e32 v125, v132, v133
	v_min3_i32 v114, v114, v123, v124
	v_mfma_f32_16x16x32_f16 v[206:209], v[78:81], v[34:37], 0
	v_min3_i32 v218, v114, v125, s11
	s_add_i32 s11, s3, 0x500
	s_mov_b32 s12, 0x2aaaaaab
	v_mfma_f32_16x16x32_f16 v[212:215], v[74:77], v[34:37], 0
	s_nop 0
	v_min3_i32 v114, v150, v151, v158
	v_min3_i32 v114, v152, v153, v114
	v_min3_i32 v114, v174, v175, v114
	v_min3_i32 v130, v176, v177, v114
	v_min3_i32 v130, v134, v135, v130
	v_min3_i32 v130, v136, v137, v130
	v_min3_i32 v130, v178, v179, v130
	v_min3_i32 v219, v180, v181, v130
	v_cmp_ge_i32_e32 vcc, v219, v158
	v_mfma_f32_16x16x32_f16 v[224:227], v[94:97], v[30:33], 0
	s_nop 0
	v_cndmask_b32_e32 v221, 1, v159, vcc
	v_mfma_f32_16x16x32_f16 v[228:231], v[78:81], v[30:33], 0
	v_mfma_f32_16x16x32_f16 v[232:235], v[74:77], v[30:33], 0
	s_nop 0
	v_min3_i32 v130, v162, v163, v170
	v_min3_i32 v130, v164, v165, v130
	v_min3_i32 v130, v182, v183, v130
	v_min3_i32 v130, v184, v185, v130
	v_min3_i32 v134, v206, v207, v130
	v_mfma_f32_16x16x32_f16 v[236:239], v[94:97], v[26:29], 0
	v_mfma_f32_16x16x32_f16 v[186:189], v[94:97], v[22:25], 0
	v_mfma_f32_16x16x32_f16 v[146:149], v[94:97], v[18:21], 0
	v_mfma_f32_16x16x32_f16 v[138:141], v[94:97], v[14:17], 0
	v_mfma_f32_16x16x32_f16 v[142:145], v[94:97], v[10:13], 0
	v_mfma_f32_16x16x32_f16 v[126:129], v[94:97], v[6:9], 0
	v_mfma_f32_16x16x32_f16 v[94:97], v[78:81], v[26:29], 0
	v_mfma_f32_16x16x32_f16 v[190:193], v[78:81], v[22:25], 0
	v_mfma_f32_16x16x32_f16 v[174:177], v[78:81], v[18:21], 0
	v_mfma_f32_16x16x32_f16 v[158:161], v[78:81], v[14:17], 0
	v_mfma_f32_16x16x32_f16 v[162:165], v[78:81], v[10:13], 0
	v_mfma_f32_16x16x32_f16 v[130:133], v[78:81], v[6:9], 0
	v_min3_i32 v78, v208, v209, v134
	v_min3_i32 v78, v212, v213, v78
	v_min3_i32 v217, v214, v215, v78
	v_cmp_ge_i32_e32 vcc, v217, v170
	v_mfma_f32_16x16x32_f16 v[122:125], v[74:77], v[26:29], 0
	s_nop 0
	v_cndmask_b32_e32 v222, 1, v171, vcc
	v_mfma_f32_16x16x32_f16 v[114:117], v[74:77], v[22:25], 0
	v_min3_i32 v78, v166, v167, v172
	v_min3_i32 v78, v168, v169, v78
	v_min3_i32 v78, v224, v225, v78
	v_min3_i32 v134, v226, v227, v78
	v_min3_i32 v134, v228, v229, v134
	v_min3_i32 v134, v230, v231, v134
	v_min3_i32 v134, v232, v233, v134
	v_min3_i32 v211, v234, v235, v134
	v_cmp_ge_i32_e32 vcc, v211, v172
	v_mfma_f32_16x16x32_f16 v[182:185], v[74:77], v[18:21], 0
	s_nop 0
	v_cndmask_b32_e32 v213, 1, v173, vcc
	v_mfma_f32_16x16x32_f16 v[178:181], v[74:77], v[14:17], 0
	v_mfma_f32_16x16x32_f16 v[78:81], v[74:77], v[10:13], 0
	v_mfma_f32_16x16x32_f16 v[150:153], v[74:77], v[6:9], 0
	v_min3_i32 v74, v154, v155, v196
	v_min3_i32 v74, v156, v157, v74
	v_min3_i32 v74, v236, v237, v74
	v_min3_i32 v74, v238, v239, v74
	v_min3_i32 v74, v94, v95, v74
	v_min3_i32 v74, v96, v97, v74
	v_min3_i32 v74, v122, v123, v74
	v_min3_i32 v212, v124, v125, v74
	v_cmp_ge_i32_e32 vcc, v212, v196
	s_waitcnt vmcnt(11)
	v_mfma_f32_16x16x32_f16 v[166:169], v[70:73], v[2:5], 0
	v_cndmask_b32_e32 v214, 1, v197, vcc
	v_mfma_f32_16x16x32_f16 v[170:173], v[70:73], v[34:37], 0
	v_min3_i32 v74, v110, v111, v194
	v_min3_i32 v74, v112, v113, v74
	v_min3_i32 v74, v186, v187, v74
	v_min3_i32 v74, v188, v189, v74
	v_min3_i32 v74, v190, v191, v74
	v_min3_i32 v74, v192, v193, v74
	v_min3_i32 v74, v114, v115, v74
	v_min3_i32 v215, v116, v117, v74
	v_cmp_ge_i32_e32 vcc, v215, v194
	v_mfma_f32_16x16x32_f16 v[154:157], v[70:73], v[30:33], 0
	s_nop 0
	v_cndmask_b32_e32 v216, 1, v195, vcc
	v_mfma_f32_16x16x32_f16 v[134:137], v[70:73], v[26:29], 0
	v_min3_i32 v74, v118, v119, v198
	v_min3_i32 v74, v120, v121, v74
	v_mfma_f32_16x16x32_f16 v[122:125], v[70:73], v[22:25], 0
	v_mfma_f32_16x16x32_f16 v[94:97], v[70:73], v[18:21], 0
	v_mfma_f32_16x16x32_f16 v[110:113], v[70:73], v[14:17], 0
	v_mfma_f32_16x16x32_f16 v[114:117], v[70:73], v[10:13], 0
	v_mfma_f32_16x16x32_f16 v[118:121], v[70:73], v[6:9], 0
	v_min3_i32 v70, v146, v147, v74
	v_min3_i32 v70, v148, v149, v70
	v_min3_i32 v70, v174, v175, v70
	v_min3_i32 v70, v176, v177, v70
	v_min3_i32 v70, v182, v183, v70
	v_min3_i32 v223, v184, v185, v70
	v_cmp_ge_i32_e32 vcc, v223, v198
	s_waitcnt vmcnt(10)
	v_mfma_f32_16x16x32_f16 v[186:189], v[66:69], v[2:5], 0
	v_cndmask_b32_e32 v244, 1, v199, vcc
	v_mfma_f32_16x16x32_f16 v[190:193], v[66:69], v[34:37], 0
	v_min3_i32 v70, v102, v103, v203
	v_min3_i32 v70, v104, v105, v70
	v_min3_i32 v70, v138, v139, v70
	v_min3_i32 v70, v140, v141, v70
	v_min3_i32 v70, v158, v159, v70
	v_min3_i32 v70, v160, v161, v70
	v_min3_i32 v70, v178, v179, v70
	v_min3_i32 v245, v180, v181, v70
	v_cmp_ge_i32_e32 vcc, v245, v203
	v_mfma_f32_16x16x32_f16 v[224:227], v[66:69], v[30:33], 0
	s_nop 0
	v_cndmask_b32_e32 v246, 1, v204, vcc
	v_mfma_f32_16x16x32_f16 v[198:201], v[66:69], v[26:29], 0
	v_min3_i32 v70, v106, v107, v202
	v_min3_i32 v70, v108, v109, v70
	v_min3_i32 v70, v142, v143, v70
	v_mfma_f32_16x16x32_f16 v[158:161], v[66:69], v[22:25], 0
	v_min3_i32 v70, v144, v145, v70
	v_min3_i32 v70, v162, v163, v70
	v_min3_i32 v70, v164, v165, v70
	v_mfma_f32_16x16x32_f16 v[146:149], v[66:69], v[18:21], 0
	v_min3_i32 v70, v78, v79, v70
	v_min3_i32 v247, v80, v81, v70
	v_cmp_ge_i32_e32 vcc, v247, v202
	v_mfma_f32_16x16x32_f16 v[138:141], v[66:69], v[14:17], 0
	s_nop 0
	v_cndmask_b32_e32 v248, 1, v205, vcc
	v_mfma_f32_16x16x32_f16 v[106:109], v[66:69], v[10:13], 0
	v_mfma_f32_16x16x32_f16 v[102:105], v[66:69], v[6:9], 0
	v_mov_b32_e32 v66, 0
	s_nop 0
	v_add_u32_e32 v72, v1, v66
	v_add_u32_e32 v66, s11, v72
	s_add_i32 s11, s3, 0x540
	v_add_u32_e32 v68, s11, v72
	s_add_i32 s11, s3, 0x580
	v_add_u32_e32 v70, s11, v72
	s_addk_i32 s3, 0x5c0
	v_ashrrev_i32_e32 v67, 31, v66
	v_ashrrev_i32_e32 v69, 31, v68
	v_ashrrev_i32_e32 v71, 31, v70
	v_add_u32_e32 v72, s3, v72
	s_waitcnt vmcnt(9)
	v_mfma_f32_16x16x32_f16 v[178:181], v[90:93], v[2:5], 0
	v_lshl_add_u64 v[66:67], v[66:67], 4, s[6:7]
	v_lshl_add_u64 v[68:69], v[68:69], 4, s[6:7]
	v_lshl_add_u64 v[70:71], v[70:71], 4, s[6:7]
	s_waitcnt vmcnt(8)
	v_mfma_f32_16x16x32_f16 v[194:197], v[86:89], v[2:5], 0
	v_ashrrev_i32_e32 v73, 31, v72
	v_lshl_add_u64 v[142:143], v[72:73], 4, s[6:7]
	global_load_dwordx4 v[78:81], v[66:67], off nt
	global_load_dwordx4 v[74:77], v[68:69], off nt
	s_nop 0
	global_load_dwordx4 v[70:73], v[70:71], off nt
	s_nop 0
	global_load_dwordx4 v[66:69], v[142:143], off nt
	v_mfma_f32_16x16x32_f16 v[228:231], v[90:93], v[34:37], 0
	v_min3_i32 v98, v98, v99, v218
	v_min3_i32 v98, v100, v101, v98
	v_min3_i32 v98, v126, v127, v98
	v_min3_i32 v98, v128, v129, v98
	v_min3_i32 v98, v130, v131, v98
	v_min3_i32 v98, v132, v133, v98
	v_min3_i32 v98, v150, v151, v98
	v_min3_i32 v249, v152, v153, v98
	v_cmp_ge_i32_e32 vcc, v249, v218
	v_mfma_f32_16x16x32_f16 v[232:235], v[86:89], v[34:37], 0
	s_mul_i32 s3, s15, 6
	v_cndmask_b32_e32 v218, 1, v220, vcc
	v_mfma_f32_16x16x32_f16 v[236:239], v[90:93], v[30:33], 0
	v_min3_i32 v98, v166, v167, v219
	s_mul_i32 s11, s2, 0x90
	v_mfma_f32_16x16x32_f16 v[206:209], v[90:93], v[26:29], 0
	v_mfma_f32_16x16x32_f16 v[182:185], v[90:93], v[22:25], 0
	v_mfma_f32_16x16x32_f16 v[174:177], v[90:93], v[18:21], 0
	v_mfma_f32_16x16x32_f16 v[162:165], v[90:93], v[14:17], 0
	v_mfma_f32_16x16x32_f16 v[142:145], v[90:93], v[10:13], 0
	v_mfma_f32_16x16x32_f16 v[126:129], v[90:93], v[6:9], 0
	v_min3_i32 v90, v168, v169, v98
	v_min3_i32 v90, v186, v187, v90
	v_min3_i32 v98, v188, v189, v90
	v_min3_i32 v98, v178, v179, v98
	v_min3_i32 v98, v180, v181, v98
	v_min3_i32 v98, v194, v195, v98
	v_min3_i32 v220, v196, v197, v98
	v_cmp_ge_i32_e32 vcc, v220, v219
	v_mfma_f32_16x16x32_f16 v[240:243], v[86:89], v[30:33], 0
	s_nop 0
	v_cndmask_b32_e32 v219, 2, v221, vcc
	v_mfma_f32_16x16x32_f16 v[90:93], v[86:89], v[26:29], 0
	v_min3_i32 v98, v170, v171, v217
	v_min3_i32 v98, v172, v173, v98
	v_min3_i32 v98, v190, v191, v98
	v_min3_i32 v98, v192, v193, v98
	v_min3_i32 v98, v228, v229, v98
	v_min3_i32 v98, v230, v231, v98
	v_min3_i32 v98, v232, v233, v98
	v_min3_i32 v221, v234, v235, v98
	v_cmp_ge_i32_e32 vcc, v221, v217
	v_mfma_f32_16x16x32_f16 v[202:205], v[86:89], v[22:25], 0
	s_nop 0
	v_cndmask_b32_e32 v217, 2, v222, vcc
	v_mfma_f32_16x16x32_f16 v[194:197], v[86:89], v[18:21], 0
	v_mfma_f32_16x16x32_f16 v[186:189], v[86:89], v[14:17], 0
	v_mfma_f32_16x16x32_f16 v[166:169], v[86:89], v[10:13], 0
	v_mfma_f32_16x16x32_f16 v[150:153], v[86:89], v[6:9], 0
	v_min3_i32 v86, v154, v155, v211
	v_min3_i32 v86, v156, v157, v86
	v_min3_i32 v86, v224, v225, v86
	v_min3_i32 v86, v226, v227, v86
	v_min3_i32 v86, v236, v237, v86
	v_min3_i32 v86, v238, v239, v86
	v_min3_i32 v86, v240, v241, v86
	v_min3_i32 v222, v242, v243, v86
	v_cmp_ge_i32_e32 vcc, v222, v211
	s_waitcnt vmcnt(11)
	v_mfma_f32_16x16x32_f16 v[170:173], v[50:53], v[2:5], 0
	v_cndmask_b32_e32 v211, 2, v213, vcc
	v_mfma_f32_16x16x32_f16 v[154:157], v[50:53], v[34:37], 0
	v_min3_i32 v86, v134, v135, v212
	v_min3_i32 v86, v136, v137, v86
	v_min3_i32 v86, v198, v199, v86
	v_min3_i32 v86, v200, v201, v86
	v_min3_i32 v86, v206, v207, v86
	v_min3_i32 v86, v208, v209, v86
	v_min3_i32 v86, v90, v91, v86
	v_min3_i32 v198, v92, v93, v86
	v_cmp_ge_i32_e32 vcc, v198, v212
	s_waitcnt vmcnt(10)
	v_mfma_f32_16x16x32_f16 v[134:137], v[46:49], v[2:5], 0
	v_cndmask_b32_e32 v199, 2, v214, vcc
	v_mfma_f32_16x16x32_f16 v[178:181], v[50:53], v[30:33], 0
	v_min3_i32 v122, v122, v123, v215
	v_min3_i32 v122, v124, v125, v122
	v_min3_i32 v122, v158, v159, v122
	v_min3_i32 v122, v160, v161, v122
	v_min3_i32 v122, v182, v183, v122
	v_min3_i32 v122, v184, v185, v122
	v_min3_i32 v122, v202, v203, v122
	v_min3_i32 v200, v204, v205, v122
	v_cmp_ge_i32_e32 vcc, v200, v215
	s_waitcnt vmcnt(9)
	v_mfma_f32_16x16x32_f16 v[158:161], v[42:45], v[2:5], 0
	v_cndmask_b32_e32 v201, 2, v216, vcc
	s_waitcnt vmcnt(8)
	v_mfma_f32_16x16x32_f16 v[182:185], v[38:41], v[2:5], 0
	v_min3_i32 v94, v94, v95, v223
	v_min3_i32 v94, v96, v97, v94
	v_min3_i32 v94, v146, v147, v94
	v_min3_i32 v94, v148, v149, v94
	v_min3_i32 v94, v174, v175, v94
	v_min3_i32 v94, v176, v177, v94
	v_min3_i32 v94, v194, v195, v94
	v_min3_i32 v202, v196, v197, v94
	v_cmp_ge_i32_e32 vcc, v202, v223
	v_mfma_f32_16x16x32_f16 v[146:149], v[46:49], v[34:37], 0
	s_nop 0
	v_cndmask_b32_e32 v203, 2, v244, vcc
	v_mfma_f32_16x16x32_f16 v[174:177], v[42:45], v[34:37], 0
	v_min3_i32 v94, v110, v111, v245
	v_min3_i32 v94, v112, v113, v94
	v_min3_i32 v94, v138, v139, v94
	v_min3_i32 v94, v140, v141, v94
	v_min3_i32 v94, v162, v163, v94
	v_min3_i32 v94, v164, v165, v94
	v_min3_i32 v94, v186, v187, v94
	v_min3_i32 v204, v188, v189, v94
	v_cmp_ge_i32_e32 vcc, v204, v245
	v_mfma_f32_16x16x32_f16 v[194:197], v[38:41], v[34:37], 0
	s_nop 0
	v_cndmask_b32_e32 v205, 2, v246, vcc
	v_mfma_f32_16x16x32_f16 v[110:113], v[46:49], v[30:33], 0
	v_min3_i32 v94, v114, v115, v247
	v_min3_i32 v94, v116, v117, v94
	v_min3_i32 v94, v106, v107, v94
	v_min3_i32 v94, v108, v109, v94
	v_min3_i32 v94, v142, v143, v94
	v_min3_i32 v94, v144, v145, v94
	v_min3_i32 v94, v166, v167, v94
	v_min3_i32 v206, v168, v169, v94
	v_cmp_ge_i32_e32 vcc, v206, v247
	v_mfma_f32_16x16x32_f16 v[190:193], v[50:53], v[26:29], 0
	s_nop 0
	v_cndmask_b32_e32 v207, 2, v248, vcc
	v_mfma_f32_16x16x32_f16 v[138:141], v[46:49], v[26:29], 0
	v_min3_i32 v114, v118, v119, v249
	v_min3_i32 v114, v120, v121, v114
	v_min3_i32 v102, v102, v103, v114
	v_min3_i32 v102, v104, v105, v102
	v_min3_i32 v102, v126, v127, v102
	v_min3_i32 v102, v128, v129, v102
	v_min3_i32 v102, v150, v151, v102
	v_min3_i32 v208, v152, v153, v102
	v_cmp_ge_i32_e32 vcc, v208, v249
	v_mfma_f32_16x16x32_f16 v[118:121], v[42:45], v[30:33], 0
	s_nop 0
	v_cndmask_b32_e32 v209, 2, v218, vcc
	v_mfma_f32_16x16x32_f16 v[126:129], v[38:41], v[30:33], 0
	v_min3_i32 v102, v170, v171, v220
	v_min3_i32 v102, v172, v173, v102
	v_min3_i32 v102, v134, v135, v102
	v_min3_i32 v102, v136, v137, v102
	v_min3_i32 v102, v158, v159, v102
	v_min3_i32 v102, v160, v161, v102
	v_min3_i32 v102, v182, v183, v102
	v_min3_i32 v182, v184, v185, v102
	v_cmp_ge_i32_e32 vcc, v182, v220
	v_mfma_f32_16x16x32_f16 v[142:145], v[42:45], v[26:29], 0
	s_nop 0
	v_cndmask_b32_e32 v183, 3, v219, vcc
	v_mfma_f32_16x16x32_f16 v[150:153], v[38:41], v[26:29], 0
	v_min3_i32 v102, v154, v155, v221
	v_min3_i32 v102, v156, v157, v102
	v_min3_i32 v102, v146, v147, v102
	v_min3_i32 v134, v148, v149, v102
	v_min3_i32 v134, v174, v175, v134
	v_min3_i32 v134, v176, v177, v134
	v_min3_i32 v134, v194, v195, v134
	v_min3_i32 v174, v196, v197, v134
	v_cmp_ge_i32_e32 vcc, v174, v221
	v_mfma_f32_16x16x32_f16 v[130:133], v[50:53], v[22:25], 0
	s_nop 0
	v_cndmask_b32_e32 v175, 3, v217, vcc
	v_mfma_f32_16x16x32_f16 v[186:189], v[46:49], v[22:25], 0
	v_min3_i32 v134, v178, v179, v222
	v_min3_i32 v134, v180, v181, v134
	v_min3_i32 v110, v110, v111, v134
	v_min3_i32 v110, v112, v113, v110
	v_min3_i32 v110, v118, v119, v110
	v_min3_i32 v110, v120, v121, v110
	v_min3_i32 v110, v126, v127, v110
	v_min3_i32 v176, v128, v129, v110
	v_cmp_ge_i32_e32 vcc, v176, v222
	v_mfma_f32_16x16x32_f16 v[166:169], v[42:45], v[22:25], 0
	s_nop 0
	v_cndmask_b32_e32 v177, 3, v211, vcc
	v_mfma_f32_16x16x32_f16 v[170:173], v[38:41], v[22:25], 0
	s_nop 0
	v_min3_i32 v118, v190, v191, v198
	v_mfma_f32_16x16x32_f16 v[162:165], v[38:41], v[18:21], 0
	v_mfma_f32_16x16x32_f16 v[146:149], v[38:41], v[14:17], 0
	v_mfma_f32_16x16x32_f16 v[126:129], v[38:41], v[10:13], 0
	v_mfma_f32_16x16x32_f16 v[110:113], v[38:41], v[6:9], 0
	v_min3_i32 v38, v192, v193, v118
	v_min3_i32 v38, v138, v139, v38
	v_min3_i32 v38, v140, v141, v38
	v_min3_i32 v38, v142, v143, v38
	v_min3_i32 v38, v144, v145, v38
	v_min3_i32 v38, v150, v151, v38
	v_min3_i32 v178, v152, v153, v38
	v_cmp_ge_i32_e32 vcc, v178, v198
	v_mfma_f32_16x16x32_f16 v[98:101], v[50:53], v[18:21], 0
	s_nop 0
	v_cndmask_b32_e32 v179, 3, v199, vcc
	v_mfma_f32_16x16x32_f16 v[122:125], v[46:49], v[18:21], 0
	v_mfma_f32_16x16x32_f16 v[158:161], v[42:45], v[18:21], 0
	s_nop 0
	v_min3_i32 v38, v130, v131, v200
	v_min3_i32 v38, v132, v133, v38
	v_min3_i32 v38, v186, v187, v38
	v_min3_i32 v38, v188, v189, v38
	v_min3_i32 v38, v166, v167, v38
	v_min3_i32 v38, v168, v169, v38
	v_min3_i32 v38, v170, v171, v38
	v_min3_i32 v166, v172, v173, v38
	v_cmp_ge_i32_e32 vcc, v166, v200
	v_mfma_f32_16x16x32_f16 v[86:89], v[50:53], v[14:17], 0
	s_nop 0
	v_cndmask_b32_e32 v167, 3, v201, vcc
	v_mfma_f32_16x16x32_f16 v[106:109], v[46:49], v[14:17], 0
	v_mfma_f32_16x16x32_f16 v[114:117], v[42:45], v[14:17], 0
	s_nop 0
	v_min3_i32 v38, v98, v99, v202
	v_min3_i32 v38, v100, v101, v38
	v_min3_i32 v38, v122, v123, v38
	v_min3_i32 v38, v124, v125, v38
	v_min3_i32 v38, v158, v159, v38
	v_min3_i32 v38, v160, v161, v38
	v_min3_i32 v122, v162, v163, v38
	v_min3_i32 v158, v164, v165, v122
	v_cmp_ge_i32_e32 vcc, v158, v202
	v_mfma_f32_16x16x32_f16 v[90:93], v[50:53], v[10:13], 0
	s_nop 0
	v_cndmask_b32_e32 v159, 3, v203, vcc
	v_mfma_f32_16x16x32_f16 v[94:97], v[46:49], v[10:13], 0
	v_mfma_f32_16x16x32_f16 v[102:105], v[42:45], v[10:13], 0
	s_nop 0
	v_min3_i32 v86, v86, v87, v204
	v_min3_i32 v122, v88, v89, v86
	v_min3_i32 v106, v106, v107, v122
	v_min3_i32 v106, v108, v109, v106
	v_min3_i32 v114, v114, v115, v106
	v_min3_i32 v114, v116, v117, v114
	v_min3_i32 v114, v146, v147, v114
	v_min3_i32 v146, v148, v149, v114
	v_cmp_ge_i32_e32 vcc, v146, v204
	v_mfma_f32_16x16x32_f16 v[50:53], v[50:53], v[6:9], 0
	s_nop 0
	v_cndmask_b32_e32 v147, 3, v205, vcc
	v_mfma_f32_16x16x32_f16 v[46:49], v[46:49], v[6:9], 0
	v_mfma_f32_16x16x32_f16 v[42:45], v[42:45], v[6:9], 0
	s_nop 0
	v_min3_i32 v90, v90, v91, v206
	v_min3_i32 v90, v92, v93, v90
	v_min3_i32 v90, v94, v95, v90
	v_min3_i32 v94, v96, v97, v90
	v_min3_i32 v94, v102, v103, v94
	v_min3_i32 v94, v104, v105, v94
	v_min3_i32 v102, v126, v127, v94
	v_min3_i32 v148, v128, v129, v102
	v_cmp_ge_i32_e32 vcc, v148, v206
	s_waitcnt vmcnt(7)
	v_mfma_f32_16x16x32_f16 v[134:137], v[82:85], v[2:5], 0
	v_cndmask_b32_e32 v149, 3, v207, vcc
	v_mfma_f32_16x16x32_f16 v[138:141], v[82:85], v[34:37], 0
	v_mfma_f32_16x16x32_f16 v[142:145], v[82:85], v[30:33], 0
	v_mfma_f32_16x16x32_f16 v[150:153], v[82:85], v[26:29], 0
	v_mfma_f32_16x16x32_f16 v[154:157], v[82:85], v[22:25], 0
	v_mfma_f32_16x16x32_f16 v[130:133], v[82:85], v[18:21], 0
	v_mfma_f32_16x16x32_f16 v[118:121], v[82:85], v[14:17], 0
	v_mfma_f32_16x16x32_f16 v[98:101], v[82:85], v[10:13], 0
	v_mfma_f32_16x16x32_f16 v[38:41], v[82:85], v[6:9], 0
	s_waitcnt vmcnt(6)
	v_mfma_f32_16x16x32_f16 v[82:85], v[62:65], v[2:5], 0
	s_waitcnt vmcnt(5)
	v_mfma_f32_16x16x32_f16 v[86:89], v[58:61], v[2:5], 0
	s_waitcnt vmcnt(4)
	v_mfma_f32_16x16x32_f16 v[106:109], v[54:57], v[2:5], 0
	s_nop 0
	v_min3_i32 v50, v50, v51, v208
	v_min3_i32 v126, v52, v53, v50
	v_min3_i32 v46, v46, v47, v126
	v_min3_i32 v46, v48, v49, v46
	v_min3_i32 v42, v42, v43, v46
	v_min3_i32 v42, v44, v45, v42
	v_min3_i32 v42, v110, v111, v42
	v_min3_i32 v160, v112, v113, v42
	v_cmp_ge_i32_e32 vcc, v160, v208
	v_mfma_f32_16x16x32_f16 v[114:117], v[62:65], v[34:37], 0
	s_nop 0
	v_cndmask_b32_e32 v161, 3, v209, vcc
	v_mfma_f32_16x16x32_f16 v[122:125], v[58:61], v[34:37], 0
	v_mfma_f32_16x16x32_f16 v[90:93], v[54:57], v[34:37], 0
	s_nop 0
	v_min3_i32 v42, v134, v135, v182
	v_min3_i32 v42, v136, v137, v42
	v_min3_i32 v42, v82, v83, v42
	v_min3_i32 v42, v84, v85, v42
	v_min3_i32 v42, v86, v87, v42
	v_min3_i32 v42, v88, v89, v42
	v_min3_i32 v42, v106, v107, v42
	v_min3_i32 v134, v108, v109, v42
	v_cmp_ge_i32_e32 vcc, v134, v182
	v_mfma_f32_16x16x32_f16 v[94:97], v[62:65], v[30:33], 0
	s_nop 0
	v_cndmask_b32_e32 v135, 4, v183, vcc
	v_mfma_f32_16x16x32_f16 v[102:105], v[58:61], v[30:33], 0
	v_mfma_f32_16x16x32_f16 v[50:53], v[54:57], v[30:33], 0
	v_mfma_f32_16x16x32_f16 v[46:49], v[62:65], v[26:29], 0
	v_mfma_f32_16x16x32_f16 v[110:113], v[62:65], v[22:25], 0
	v_mfma_f32_16x16x32_f16 v[126:129], v[62:65], v[18:21], 0
	v_mfma_f32_16x16x32_f16 v[82:85], v[62:65], v[14:17], 0
	v_mfma_f32_16x16x32_f16 v[86:89], v[62:65], v[10:13], 0
	v_mfma_f32_16x16x32_f16 v[42:45], v[62:65], v[6:9], 0
	v_min3_i32 v62, v138, v139, v174
	v_min3_i32 v106, v140, v141, v62
	v_min3_i32 v106, v114, v115, v106
	v_min3_i32 v106, v116, v117, v106
	v_min3_i32 v114, v122, v123, v106
	v_min3_i32 v114, v124, v125, v114
	v_min3_i32 v90, v90, v91, v114
	v_min3_i32 v122, v92, v93, v90
	v_cmp_ge_i32_e32 vcc, v122, v174
	v_mfma_f32_16x16x32_f16 v[62:65], v[58:61], v[26:29], 0
	s_nop 0
	v_cndmask_b32_e32 v123, 4, v175, vcc
	v_mfma_f32_16x16x32_f16 v[106:109], v[54:57], v[26:29], 0
	s_nop 0
	v_min3_i32 v124, v142, v143, v176
	v_min3_i32 v124, v144, v145, v124
	v_min3_i32 v94, v94, v95, v124
	v_min3_i32 v124, v96, v97, v94
	v_min3_i32 v102, v102, v103, v124
	v_min3_i32 v102, v104, v105, v102
	v_min3_i32 v50, v50, v51, v102
	v_min3_i32 v124, v52, v53, v50
	v_cmp_ge_i32_e32 vcc, v124, v176
	v_mfma_f32_16x16x32_f16 v[90:93], v[58:61], v[22:25], 0
	s_nop 0
	v_cndmask_b32_e32 v125, 4, v177, vcc
	v_mfma_f32_16x16x32_f16 v[114:117], v[54:57], v[22:25], 0
	s_nop 0
	v_min3_i32 v136, v150, v151, v178
	v_min3_i32 v136, v152, v153, v136
	v_min3_i32 v46, v46, v47, v136
	v_min3_i32 v46, v48, v49, v46
	v_min3_i32 v62, v62, v63, v46
	v_min3_i32 v62, v64, v65, v62
	v_min3_i32 v62, v106, v107, v62
	v_min3_i32 v136, v108, v109, v62
	v_cmp_ge_i32_e32 vcc, v136, v178
	v_mfma_f32_16x16x32_f16 v[94:97], v[58:61], v[18:21], 0
	s_nop 0
	v_cndmask_b32_e32 v137, 4, v179, vcc
	v_mfma_f32_16x16x32_f16 v[46:49], v[54:57], v[18:21], 0
	s_nop 0
	v_min3_i32 v138, v154, v155, v166
	v_min3_i32 v138, v156, v157, v138
	v_min3_i32 v110, v110, v111, v138
	v_min3_i32 v110, v112, v113, v110
	v_min3_i32 v90, v90, v91, v110
	v_min3_i32 v90, v92, v93, v90
	v_min3_i32 v110, v114, v115, v90
	v_min3_i32 v138, v116, v117, v110
	v_cmp_ge_i32_e32 vcc, v138, v166
	v_mfma_f32_16x16x32_f16 v[102:105], v[58:61], v[14:17], 0
	v_mov_b32_e32 v154, 0
	v_cndmask_b32_e32 v139, 4, v167, vcc
	v_mfma_f32_16x16x32_f16 v[62:65], v[54:57], v[14:17], 0
	s_nop 0
	v_min3_i32 v114, v130, v131, v158
	v_min3_i32 v130, v132, v133, v114
	v_min3_i32 v126, v126, v127, v130
	v_min3_i32 v126, v128, v129, v126
	v_min3_i32 v94, v94, v95, v126
	v_min3_i32 v94, v96, v97, v94
	v_min3_i32 v46, v46, v47, v94
	v_min3_i32 v126, v48, v49, v46
	v_cmp_ge_i32_e32 vcc, v126, v158
	v_mfma_f32_16x16x32_f16 v[50:53], v[58:61], v[10:13], 0
	s_nop 0
	v_cndmask_b32_e32 v127, 4, v159, vcc
	v_mfma_f32_16x16x32_f16 v[106:109], v[54:57], v[10:13], 0
	s_nop 0
	v_min3_i32 v118, v118, v119, v146
	v_min3_i32 v118, v120, v121, v118
	v_min3_i32 v82, v82, v83, v118
	v_min3_i32 v118, v84, v85, v82
	v_min3_i32 v102, v102, v103, v118
	v_min3_i32 v102, v104, v105, v102
	v_min3_i32 v62, v62, v63, v102
	v_min3_i32 v102, v64, v65, v62
	v_cmp_ge_i32_e32 vcc, v102, v146
	v_mfma_f32_16x16x32_f16 v[58:61], v[58:61], v[6:9], 0
	v_and_b32_e32 v146, 7, v0
	v_cndmask_b32_e32 v103, 4, v147, vcc
	v_mfma_f32_16x16x32_f16 v[54:57], v[54:57], v[6:9], 0
	s_nop 0
	v_min3_i32 v98, v98, v99, v148
	v_min3_i32 v104, v100, v101, v98
	v_min3_i32 v86, v86, v87, v104
	v_min3_i32 v86, v88, v89, v86
	v_min3_i32 v50, v50, v51, v86
	v_min3_i32 v50, v52, v53, v50
	v_min3_i32 v50, v106, v107, v50
	v_min3_i32 v104, v108, v109, v50
	v_cmp_ge_i32_e32 vcc, v104, v148
	s_waitcnt vmcnt(3)
	v_mfma_f32_16x16x32_f16 v[90:93], v[78:81], v[2:5], 0
	v_cndmask_b32_e32 v105, 4, v149, vcc
	s_waitcnt vmcnt(2)
	v_mfma_f32_16x16x32_f16 v[110:113], v[74:77], v[2:5], 0
	s_waitcnt vmcnt(1)
	v_mfma_f32_16x16x32_f16 v[114:117], v[70:73], v[2:5], 0
	s_waitcnt vmcnt(0)
	v_mfma_f32_16x16x32_f16 v[2:5], v[66:69], v[2:5], 0
	s_nop 0
	v_min3_i32 v38, v38, v39, v160
	v_min3_i32 v38, v40, v41, v38
	v_min3_i32 v38, v42, v43, v38
	v_min3_i32 v42, v44, v45, v38
	v_min3_i32 v42, v58, v59, v42
	v_min3_i32 v42, v60, v61, v42
	v_min3_i32 v54, v54, v55, v42
	v_min3_i32 v106, v56, v57, v54
	v_cmp_ge_i32_e32 vcc, v106, v160
	v_mfma_f32_16x16x32_f16 v[46:49], v[78:81], v[34:37], 0
	s_nop 0
	v_cndmask_b32_e32 v107, 4, v161, vcc
	v_mfma_f32_16x16x32_f16 v[94:97], v[74:77], v[34:37], 0
	v_mfma_f32_16x16x32_f16 v[82:85], v[70:73], v[34:37], 0
	v_mfma_f32_16x16x32_f16 v[34:37], v[66:69], v[34:37], 0
	s_nop 0
	v_min3_i32 v54, v90, v91, v134
	v_min3_i32 v58, v92, v93, v54
	v_min3_i32 v58, v110, v111, v58
	v_min3_i32 v58, v112, v113, v58
	v_min3_i32 v90, v114, v115, v58
	v_min3_i32 v90, v116, v117, v90
	v_min3_i32 v2, v2, v3, v90
	v_min3_i32 v91, v4, v5, v2
	v_cmp_ge_i32_e32 vcc, v91, v134
	v_mfma_f32_16x16x32_f16 v[62:65], v[78:81], v[30:33], 0
	s_nop 0
	v_cndmask_b32_e32 v90, 5, v135, vcc
	v_add_u32_e32 v251, s3, v90
	v_lshl_or_b32 v90, v251, 2, v253
	ds_min_u64 v252, v[90:91] offset:16384
	v_mfma_f32_16x16x32_f16 v[98:101], v[74:77], v[30:33], 0
	v_mfma_f32_16x16x32_f16 v[86:89], v[70:73], v[30:33], 0
	v_mfma_f32_16x16x32_f16 v[30:33], v[66:69], v[30:33], 0
	s_nop 0
	v_min3_i32 v46, v46, v47, v122
	v_min3_i32 v46, v48, v49, v46
	v_min3_i32 v46, v94, v95, v46
	v_min3_i32 v92, v96, v97, v46
	v_min3_i32 v82, v82, v83, v92
	v_min3_i32 v82, v84, v85, v82
	v_min3_i32 v34, v34, v35, v82
	v_min3_i32 v93, v36, v37, v34
	v_cmp_ge_i32_e32 vcc, v93, v122
	v_mfma_f32_16x16x32_f16 v[50:53], v[78:81], v[26:29], 0
	s_nop 0
	v_cndmask_b32_e32 v92, 5, v123, vcc
	v_add_u32_e32 v251, s3, v92
	v_lshl_or_b32 v92, v251, 2, v253
	ds_min_u64 v252, v[92:93] offset:16512
	v_mfma_f32_16x16x32_f16 v[38:41], v[74:77], v[26:29], 0
	v_mfma_f32_16x16x32_f16 v[42:45], v[70:73], v[26:29], 0
	v_mfma_f32_16x16x32_f16 v[26:29], v[66:69], v[26:29], 0
	s_nop 0
	v_min3_i32 v62, v62, v63, v124
	v_min3_i32 v62, v64, v65, v62
	v_min3_i32 v62, v98, v99, v62
	v_min3_i32 v62, v100, v101, v62
	v_min3_i32 v86, v86, v87, v62
	v_min3_i32 v86, v88, v89, v86
	v_min3_i32 v30, v30, v31, v86
	v_min3_i32 v95, v32, v33, v30
	v_cmp_ge_i32_e32 vcc, v95, v124
	v_mfma_f32_16x16x32_f16 v[54:57], v[78:81], v[22:25], 0
	s_nop 0
	v_cndmask_b32_e32 v94, 5, v125, vcc
	v_add_u32_e32 v251, s3, v94
	v_lshl_or_b32 v94, v251, 2, v253
	ds_min_u64 v252, v[94:95] offset:16640
	v_mfma_f32_16x16x32_f16 v[58:61], v[74:77], v[22:25], 0
	v_mfma_f32_16x16x32_f16 v[2:5], v[70:73], v[22:25], 0
	v_mfma_f32_16x16x32_f16 v[22:25], v[66:69], v[22:25], 0
	s_nop 0
	v_min3_i32 v50, v50, v51, v136
	v_min3_i32 v50, v52, v53, v50
	v_min3_i32 v38, v38, v39, v50
	v_min3_i32 v38, v40, v41, v38
	v_min3_i32 v38, v42, v43, v38
	v_min3_i32 v38, v44, v45, v38
	v_min3_i32 v26, v26, v27, v38
	v_min3_i32 v51, v28, v29, v26
	v_cmp_ge_i32_e32 vcc, v51, v136
	v_mfma_f32_16x16x32_f16 v[46:49], v[78:81], v[18:21], 0
	s_nop 0
	v_cndmask_b32_e32 v50, 5, v137, vcc
	v_add_u32_e32 v251, s3, v50
	v_lshl_or_b32 v50, v251, 2, v253
	ds_min_u64 v252, v[50:51] offset:16768
	v_mfma_f32_16x16x32_f16 v[82:85], v[74:77], v[18:21], 0
	v_mfma_f32_16x16x32_f16 v[34:37], v[70:73], v[18:21], 0
	v_mfma_f32_16x16x32_f16 v[18:21], v[66:69], v[18:21], 0
	s_nop 0
	v_min3_i32 v42, v54, v55, v138
	v_min3_i32 v52, v56, v57, v42
	v_min3_i32 v52, v58, v59, v52
	v_min3_i32 v52, v60, v61, v52
	v_min3_i32 v2, v2, v3, v52
	v_min3_i32 v2, v4, v5, v2
	v_min3_i32 v2, v22, v23, v2
	v_min3_i32 v53, v24, v25, v2
	v_cmp_ge_i32_e32 vcc, v53, v138
	v_mfma_f32_16x16x32_f16 v[62:65], v[78:81], v[14:17], 0
	s_nop 0
	v_cndmask_b32_e32 v52, 5, v139, vcc
	v_add_u32_e32 v251, s3, v52
	v_lshl_or_b32 v52, v251, 2, v253
	ds_min_u64 v252, v[52:53] offset:16896
	v_mfma_f32_16x16x32_f16 v[30:33], v[74:77], v[14:17], 0
	v_mfma_f32_16x16x32_f16 v[86:89], v[70:73], v[14:17], 0
	v_mfma_f32_16x16x32_f16 v[14:17], v[66:69], v[14:17], 0
	s_nop 0
	v_min3_i32 v46, v46, v47, v126
	v_min3_i32 v46, v48, v49, v46
	v_min3_i32 v54, v82, v83, v46
	v_min3_i32 v54, v84, v85, v54
	v_min3_i32 v34, v34, v35, v54
	v_min3_i32 v34, v36, v37, v34
	v_min3_i32 v18, v18, v19, v34
	v_min3_i32 v19, v20, v21, v18
	v_cmp_ge_i32_e32 vcc, v19, v126
	v_mfma_f32_16x16x32_f16 v[38:41], v[78:81], v[10:13], 0
	s_nop 0
	v_cndmask_b32_e32 v18, 5, v127, vcc
	v_add_u32_e32 v251, s3, v18
	v_lshl_or_b32 v18, v251, 2, v253
	ds_min_u64 v252, v[18:19] offset:17024
	v_mfma_f32_16x16x32_f16 v[26:29], v[74:77], v[10:13], 0
	v_mfma_f32_16x16x32_f16 v[42:45], v[70:73], v[10:13], 0
	v_mfma_f32_16x16x32_f16 v[10:13], v[66:69], v[10:13], 0
	s_nop 0
	v_min3_i32 v20, v62, v63, v102
	v_min3_i32 v20, v64, v65, v20
	v_min3_i32 v20, v30, v31, v20
	v_min3_i32 v20, v32, v33, v20
	v_min3_i32 v20, v86, v87, v20
	v_min3_i32 v20, v88, v89, v20
	v_min3_i32 v14, v14, v15, v20
	v_min3_i32 v15, v16, v17, v14
	v_cmp_ge_i32_e32 vcc, v15, v102
	v_mfma_f32_16x16x32_f16 v[2:5], v[78:81], v[6:9], 0
	v_bfe_u32 v17, v0, 4, 2
	v_cndmask_b32_e32 v14, 5, v103, vcc
	v_add_u32_e32 v251, s3, v14
	v_lshl_or_b32 v14, v251, 2, v253
	ds_min_u64 v252, v[14:15] offset:17152
	v_mfma_f32_16x16x32_f16 v[22:25], v[74:77], v[6:9], 0
	v_mfma_f32_16x16x32_f16 v[46:49], v[70:73], v[6:9], 0
	v_mfma_f32_16x16x32_f16 v[6:9], v[66:69], v[6:9], 0
	s_nop 0
	v_min3_i32 v16, v38, v39, v104
	v_min3_i32 v16, v40, v41, v16
	v_min3_i32 v16, v26, v27, v16
	v_min3_i32 v2, v2, v3, v106
	v_min3_i32 v16, v28, v29, v16
	v_min3_i32 v2, v4, v5, v2
	v_min3_i32 v16, v42, v43, v16
	v_min3_i32 v2, v22, v23, v2
	v_lshlrev_b32_e32 v4, 3, v210
	v_min3_i32 v16, v44, v45, v16
	v_min3_i32 v2, v24, v25, v2
	v_min3_i32 v10, v10, v11, v16
	v_min3_i32 v2, v46, v47, v2
	v_min3_i32 v11, v12, v13, v10
	v_min3_i32 v2, v48, v49, v2
	v_cmp_ge_i32_e32 vcc, v11, v104
	v_min3_i32 v2, v6, v7, v2
	v_cndmask_b32_e32 v10, 5, v105, vcc
	v_add_u32_e32 v251, s3, v10
	v_lshl_or_b32 v10, v251, 2, v253
	ds_min_u64 v252, v[10:11] offset:17280
	v_min3_i32 v3, v8, v9, v2
	v_cmp_ge_i32_e32 vcc, v3, v106
	v_cndmask_b32_e32 v2, 5, v107, vcc
	v_add_u32_e32 v2, s3, v2
	v_bfe_u32 v10, v0, 3, 3
	s_lshl_b32 s3, s15, 3
	v_lshl_or_b32 v2, v2, 2, v17
	v_or_b32_e32 v151, s3, v10
	ds_min_u64 v4, v[2:3] offset:17408
	v_lshlrev_b32_e32 v2, 3, v151
	s_waitcnt lgkmcnt(0)
	s_barrier
	ds_read2st64_b32 v[4:5], v2 offset0:64 offset1:66
	s_add_i32 s2, s3, s11
	s_lshr_b32 s2, s2, 4
	s_add_i32 s2, s2, s8
	s_waitcnt lgkmcnt(0)
	v_ashrrev_i32_e32 v3, 2, v4
	v_mul_hi_i32 v6, v3, s12
	v_lshrrev_b32_e32 v7, 31, v6
	v_add_u32_e32 v6, v6, v7
	v_mul_lo_u32 v7, v6, -6
	v_mul_lo_u32 v6, v6, 24
	v_min_i32_e32 v6, 0xa5, v6
	v_add_lshl_u32 v7, v7, v3, 2
	v_bfe_u32 v3, v0, 2, 1
	v_add3_u32 v152, v6, v3, v7
	v_lshlrev_b32_e32 v6, 2, v4
	v_and_b32_e32 v4, 3, v0
	v_and_or_b32 v153, v6, 12, v4
	v_add_u32_e32 v6, s9, v152
	v_lshl_or_b32 v6, v6, 6, v153
	v_bitop3_b32 v7, s3, 15, v10 bitop3:0xc8
	v_lshl_or_b32 v8, s2, 6, v7
	v_ashrrev_i32_e32 v7, 31, v6
	v_lshl_add_u64 v[6:7], v[6:7], 4, s[6:7]
	v_ashrrev_i32_e32 v9, 31, v8
	v_lshl_add_u64 v[8:9], v[8:9], 4, s[4:5]
	global_load_dwordx4 v[126:129], v[6:7], off
	global_load_dwordx4 v[114:117], v[6:7], off offset:256
	global_load_dwordx4 v[130:133], v[6:7], off offset:2048
	global_load_dwordx4 v[118:121], v[6:7], off offset:2304
	global_load_dwordx4 v[134:137], v[8:9], off
	global_load_dwordx4 v[122:125], v[8:9], off offset:256
	global_load_dwordx4 v[102:105], v[6:7], off offset:512
	global_load_dwordx4 v[78:81], v[6:7], off offset:768
	global_load_dwordx4 v[106:109], v[6:7], off offset:2560
	global_load_dwordx4 v[82:85], v[6:7], off offset:2816
	v_ashrrev_i32_e32 v6, 2, v5
	v_mul_hi_i32 v7, v6, s12
	v_lshrrev_b32_e32 v11, 31, v7
	v_add_u32_e32 v7, v7, v11
	v_mul_lo_u32 v11, v7, -6
	v_mul_lo_u32 v7, v7, 24
	s_add_i32 s2, s3, 64
	v_min_i32_e32 v7, 0xa5, v7
	v_add_lshl_u32 v6, v11, v6, 2
	s_add_i32 s3, s2, s11
	v_add3_u32 v148, v7, v3, v6
	v_lshlrev_b32_e32 v5, 2, v5
	v_and_or_b32 v149, v5, 12, v4
	v_add_u32_e32 v5, s9, v148
	s_lshr_b32 s3, s3, 4
	v_lshl_or_b32 v6, v5, 6, v149
	s_add_i32 s3, s3, s8
	v_bitop3_b32 v5, s2, 15, v10 bitop3:0xc8
	v_lshl_or_b32 v10, s3, 6, v5
	v_ashrrev_i32_e32 v7, 31, v6
	v_ashrrev_i32_e32 v11, 31, v10
	v_lshl_add_u64 v[6:7], v[6:7], 4, s[6:7]
	v_lshl_add_u64 v[10:11], v[10:11], 4, s[4:5]
	global_load_dwordx4 v[142:145], v[8:9], off offset:512
	global_load_dwordx4 v[138:141], v[8:9], off offset:768
	global_load_dwordx4 v[90:93], v[6:7], off
	global_load_dwordx4 v[62:65], v[6:7], off offset:256
	global_load_dwordx4 v[94:97], v[6:7], off offset:2048
	global_load_dwordx4 v[66:69], v[6:7], off offset:2304
	global_load_dwordx4 v[38:41], v[6:7], off offset:512
	global_load_dwordx4 v[18:21], v[6:7], off offset:768
	global_load_dwordx4 v[42:45], v[6:7], off offset:2560
	global_load_dwordx4 v[22:25], v[6:7], off offset:2816
	global_load_dwordx4 v[110:113], v[10:11], off
	global_load_dwordx4 v[86:89], v[10:11], off offset:256
	global_load_dwordx4 v[54:57], v[10:11], off offset:512
	global_load_dwordx4 v[26:29], v[10:11], off offset:768
	s_cmpk_lt_u32 s10, 0x80
	s_cselect_b64 s[2:3], -1, 0
	s_cmpk_gt_u32 s10, 0x7f
	s_cbranch_scc1 .LBB1_4
	v_add_u32_e32 v2, 0x4000, v2
	ds_read_b32 v2, v2 offset:1024
	v_or_b32_e32 v147, 0x80, v151
	v_add_u32_e32 v5, s11, v147
	s_waitcnt lgkmcnt(0)
	v_ashrrev_i32_e32 v6, 2, v2
	v_mul_hi_i32 v7, v6, s12
	v_lshrrev_b32_e32 v8, 31, v7
	v_add_u32_e32 v7, v7, v8
	v_mul_lo_u32 v8, v7, -6
	v_mul_lo_u32 v7, v7, 24
	v_min_i32_e32 v7, 0xa5, v7
	v_add_lshl_u32 v6, v8, v6, 2
	v_add3_u32 v150, v7, v3, v6
	v_lshlrev_b32_e32 v2, 2, v2
	v_lshrrev_b32_e32 v3, 4, v5
	v_and_or_b32 v155, v2, 12, v4
	v_add_u32_e32 v2, s9, v150
	v_add_u32_e32 v3, s8, v3
	v_lshl_or_b32 v2, v2, 6, v155
	v_lshl_or_b32 v4, v3, 6, v151
	v_ashrrev_i32_e32 v3, 31, v2
	v_ashrrev_i32_e32 v5, 31, v4
	v_lshl_add_u64 v[2:3], v[2:3], 4, s[6:7]
	v_lshl_add_u64 v[50:51], v[4:5], 4, s[4:5]
	global_load_dwordx4 v[58:61], v[2:3], off
	global_load_dwordx4 v[46:49], v[2:3], off offset:256
	global_load_dwordx4 v[34:37], v[2:3], off offset:2048
	global_load_dwordx4 v[10:13], v[2:3], off offset:2304
	global_load_dwordx4 v[98:101], v[50:51], off
	global_load_dwordx4 v[74:77], v[50:51], off offset:256
	global_load_dwordx4 v[30:33], v[2:3], off offset:512
	global_load_dwordx4 v[14:17], v[2:3], off offset:768
	global_load_dwordx4 v[6:9], v[2:3], off offset:2560
	s_nop 0
	global_load_dwordx4 v[2:5], v[2:3], off offset:2816
	s_nop 0
	global_load_dwordx4 v[70:73], v[50:51], off offset:512
	s_nop 0
	global_load_dwordx4 v[50:53], v[50:51], off offset:768
	v_lshl_or_b32 v150, v150, 4, v155
	s_branch .LBB1_5

.LBB1_22:
	s_or_b64 exec, exec, s[8:9]
	v_lshl_add_u32 v5, v3, 1, v3
	v_mad_u64_u32 v[10:11], s[0:1], v2, v5, 0
	v_ashrrev_i32_e32 v12, 31, v5
	v_mov_b32_e32 v6, v11
	v_mad_u64_u32 v[12:13], s[0:1], v2, v12, v[6:7]
	v_mov_b32_e32 v11, v12
	v_lshl_add_u32 v4, v4, 1, v4
	v_lshl_add_u64 v[8:9], v[10:11], 2, v[8:9]
	v_ashrrev_i32_e32 v5, 31, v4
	v_mov_b32_e32 v3, 0
	v_lshl_add_u64 v[24:25], v[4:5], 2, v[8:9]
	v_lshl_add_u64 v[12:13], v[2:3], 2, v[24:25]
	global_load_dwordx3 v[4:6], v[24:25], off
	global_load_dwordx3 v[8:10], v[12:13], off
	v_lshlrev_b32_e32 v26, 1, v2
	v_mov_b32_e32 v27, v3
	v_lshl_add_u64 v[12:13], v[26:27], 2, v[24:25]
	global_load_dwordx3 v[12:14], v[12:13], off
	v_mul_u32_u24_e32 v16, v2, v2
	v_mov_b32_e32 v17, v3
	v_lshl_add_u64 v[20:21], v[16:17], 2, v[24:25]
	global_load_dwordx3 v[16:18], v[20:21], off
	v_ashrrev_i32_e32 v23, 31, v2
	v_mov_b32_e32 v22, v2
	v_mul_u32_u24_e32 v2, v26, v2
	v_lshlrev_b64 v[36:37], 2, v[22:23]
	v_lshl_add_u64 v[2:3], v[2:3], 2, v[24:25]
	v_lshl_add_u64 v[28:29], v[20:21], 0, v[36:37]
	global_load_dwordx3 v[24:26], v[2:3], off
	v_lshl_add_u64 v[2:3], v[2:3], 0, v[36:37]
	global_load_dwordx3 v[32:34], v[2:3], off
	global_load_dwordx3 v[20:22], v[28:29], off
	v_lshl_add_u64 v[28:29], v[28:29], 0, v[36:37]
	global_load_dwordx3 v[28:30], v[28:29], off
	v_lshl_add_u64 v[2:3], v[2:3], 0, v[36:37]
	global_load_dwordx3 v[36:38], v[2:3], off
	v_mul_lo_u16_e32 v2, 0xab, v7
	s_movk_i32 s0, 0xffd0
	v_lshrrev_b16_e32 v2, 13, v2
	v_mad_i32_i24 v3, v2, s0, v7
	s_movk_i32 s1, 0x6c0
	v_mul_lo_u32 v3, v3, 12
	v_mad_u32_u24 v7, v2, s1, v3
	ds_read2_b32 v[2:3], v7 offset0:2 offset1:146
	ds_read2_b32 v[40:41], v7 offset1:1
	ds_read2_b32 v[42:43], v7 offset0:144 offset1:145
	ds_read_b32 v31, v7 offset:1160
	ds_read_b32 v35, v7 offset:6344
	v_add_u32_e32 v19, 0x1400, v7
	v_add_u32_e32 v46, 0x2800, v7
	v_add_u32_e32 v52, 0x2ac0, v7
	v_add_u32_e32 v54, 0x2d00, v7
	v_add_u32_e32 v11, 0x480, v7
	v_add_u32_e32 v15, 0x1440, v7
	v_add_u32_e32 v23, 0x1680, v7
	v_add_u32_e32 v27, 0x18c0, v7
	v_add_u32_e32 v39, 0x2880, v7
	ds_read2_b32 v[44:45], v19 offset0:18 offset1:162
	ds_read2_b32 v[46:47], v46 offset0:34 offset1:178
	ds_read2_b32 v[48:49], v27 offset1:1
	ds_read2_b32 v[50:51], v39 offset1:1
	ds_read2_b32 v[52:53], v52 offset1:1
	ds_read2_b32 v[54:55], v54 offset1:1
	ds_read2_b32 v[56:57], v11 offset1:1
	ds_read2_b32 v[58:59], v15 offset1:1
	ds_read2_b32 v[60:61], v23 offset1:1
	ds_read_b32 v7, v7 offset:11528
	s_movk_i32 s0, 0x90
	v_cmp_gt_u32_e32 vcc, s0, v0
	s_waitcnt vmcnt(8) lgkmcnt(13)
	v_sub_f32_e32 v4, v40, v4
	v_sub_f32_e32 v5, v41, v5
	v_sub_f32_e32 v2, v2, v6
	v_add_f32_e64 v4, |v4|, |v5|
	s_waitcnt vmcnt(7) lgkmcnt(12)
	v_sub_f32_e32 v5, v42, v8
	v_add_f32_e64 v2, v4, |v2|
	v_sub_f32_e32 v6, v43, v9
	v_add_f32_e64 v2, v2, |v5|
	v_sub_f32_e32 v3, v3, v10
	v_add_f32_e64 v2, v2, |v6|
	s_waitcnt vmcnt(6) lgkmcnt(3)
	v_sub_f32_e32 v8, v56, v12
	v_add_f32_e64 v2, v2, |v3|
	v_sub_f32_e32 v9, v57, v13
	v_add_f32_e64 v2, v2, |v8|
	v_sub_f32_e32 v10, v31, v14
	v_add_f32_e64 v2, v2, |v9|
	s_waitcnt vmcnt(5) lgkmcnt(2)
	v_sub_f32_e32 v11, v58, v16
	v_add_f32_e64 v2, v2, |v10|
	v_sub_f32_e32 v12, v59, v17
	v_add_f32_e64 v2, v2, |v11|
	v_sub_f32_e32 v13, v44, v18
	v_add_f32_e64 v2, v2, |v12|
	s_waitcnt vmcnt(2) lgkmcnt(1)
	v_sub_f32_e32 v4, v60, v20
	v_add_f32_e64 v2, v2, |v13|
	v_sub_f32_e32 v14, v61, v21
	v_add_f32_e64 v2, v2, |v4|
	v_sub_f32_e32 v15, v45, v22
	v_add_f32_e64 v2, v2, |v14|
	s_waitcnt vmcnt(1)
	v_sub_f32_e32 v5, v48, v28
	v_add_f32_e64 v2, v2, |v15|
	v_sub_f32_e32 v17, v49, v29
	v_add_f32_e64 v2, v2, |v5|
	v_sub_f32_e32 v18, v35, v30
	v_add_f32_e64 v2, v2, |v17|
	v_sub_f32_e32 v16, v50, v24
	v_add_f32_e64 v2, v2, |v18|
	v_add_f32_e64 v2, v2, |v16|
	v_sub_f32_e32 v3, v51, v25
	v_add_f32_e64 v2, v2, |v3|
	v_sub_f32_e32 v3, v46, v26
	v_add_f32_e64 v2, v2, |v3|
	v_sub_f32_e32 v3, v52, v32
	v_add_f32_e64 v2, v2, |v3|
	v_sub_f32_e32 v3, v53, v33
	v_add_f32_e64 v2, v2, |v3|
	v_sub_f32_e32 v3, v47, v34
	v_add_f32_e64 v2, v2, |v3|
	s_waitcnt vmcnt(0)
	v_sub_f32_e32 v3, v54, v36
	v_add_f32_e64 v2, v2, |v3|
	v_sub_f32_e32 v3, v55, v37
	v_add_f32_e64 v2, v2, |v3|
	s_waitcnt lgkmcnt(0)
	v_sub_f32_e32 v3, v7, v38
	v_add_f32_e64 v2, v2, |v3|
	v_cndmask_b32_e32 v2, 0, v2, vcc
	s_nop 1
	v_add_f32_dpp v2, v2, v2 quad_perm:[1,0,3,2] row_mask:0xf bank_mask:0xf
	s_nop 1
	v_add_f32_dpp v2, v2, v2 quad_perm:[2,3,0,1] row_mask:0xf bank_mask:0xf
	s_nop 1
	v_add_f32_dpp v2, v2, v2 row_half_mirror row_mask:0xf bank_mask:0xf
	s_nop 1
	v_add_f32_dpp v2, v2, v2 row_mirror row_mask:0xf bank_mask:0xf
	s_nop 1
	v_add_f32_dpp v2, v2, v2 row_bcast:15 row_mask:0xa bank_mask:0xf
	s_nop 1
	v_add_f32_dpp v2, v2, v2 row_bcast:31 row_mask:0xc bank_mask:0xf
	v_mov_b32_e32 v3, 0
	v_cmp_eq_u32_e32 vcc, 63, v1
	s_and_b64 exec, exec, vcc
	s_cbranch_execz .LBB1_24
	s_lshl_b32 s0, s15, 2
	s_waitcnt lgkmcnt(0)
	v_add_f32_e32 v1, v2, v3
	v_mov_b32_e32 v2, s0
	ds_write_b32 v2, v1 offset:18112
